# edge_main LayerNorm: one-pass sum and sum-of-squares, cross-lane reduce with permlane16/32 swaps instead of 4 ds_bpermute round trips
# speedup vs baseline: 1.0300x; 1.0201x over previous
.LBB1_6:
	s_waitcnt vmcnt(14)
	ds_write_b128 v119, v[38:41]
	s_waitcnt vmcnt(13)
	ds_write_b128 v119, v[42:45] offset:2304
	s_waitcnt vmcnt(12)
	ds_write_b128 v119, v[46:49] offset:4608
	s_waitcnt vmcnt(11)
	ds_write_b128 v119, v[50:53] offset:6912
	ds_bpermute_b32 v42, v107, v64
	ds_bpermute_b32 v43, v109, v64
	ds_bpermute_b32 v44, v110, v64
	v_add_u32_e32 v0, 0x1000, v62
	ds_bpermute_b32 v50, v111, v64
	v_min_i32_e32 v0, 0x927b, v0
	v_lshl_or_b32 v40, v0, 4, v106
	s_waitcnt lgkmcnt(3)
	v_lshlrev_b32_e32 v0, 7, v42
	v_ashrrev_i32_e32 v65, 31, v64
	v_lshl_add_u64 v[46:47], v[98:99], 0, v[0:1]
	s_waitcnt lgkmcnt(2)
	v_lshlrev_b32_e32 v0, 7, v43
	v_lshl_add_u64 v[38:39], v[64:65], 2, v[96:97]
	v_ashrrev_i32_e32 v41, 31, v40
	v_lshl_add_u64 v[48:49], v[98:99], 0, v[0:1]
	s_waitcnt lgkmcnt(1)
	v_lshlrev_b32_e32 v0, 7, v44
	s_waitcnt vmcnt(10)
	ds_bpermute_b32 v68, v114, v108
	ds_bpermute_b32 v66, v115, v108
	global_load_dword v108, v[38:39], off
	v_lshl_add_u64 v[38:39], v[40:41], 2, v[94:95]
	v_lshl_add_u64 v[64:65], v[100:101], 0, v[0:1]
	s_waitcnt lgkmcnt(2)
	v_lshlrev_b32_e32 v0, 7, v50
	global_load_dword v135, v[38:39], off
	s_nop 0
	global_load_dwordx4 v[38:41], v[46:47], off
	global_load_dwordx4 v[42:45], v[48:49], off
	v_lshl_add_u64 v[70:71], v[100:101], 0, v[0:1]
	global_load_dwordx4 v[46:49], v[64:65], off
	global_load_dwordx4 v[50:53], v[70:71], off
	ds_read_b128 v[70:73], v120
	ds_read_b128 v[74:77], v120 offset:64
	ds_read_b128 v[78:81], v120 offset:4608
	ds_read_b128 v[82:85], v120 offset:4672
	v_add_u32_e32 v0, 0x800, v62
	ds_write_b128 v121, v[2:5]
	ds_write_b128 v121, v[6:9] offset:1088
	ds_write_b128 v121, v[10:13] offset:2176
	ds_write_b128 v121, v[14:17] offset:3264
	ds_write_b128 v121, v[18:21] offset:4352
	ds_write_b128 v121, v[22:25] offset:5440
	s_waitcnt vmcnt(15)
	ds_write_b128 v121, v[26:29] offset:6528
	s_waitcnt vmcnt(14)
	ds_write_b128 v121, v[30:33] offset:7616
	ds_write_b128 v122, v[34:37] offset:8704
	v_min_i32_e32 v2, 0x927b, v0
	v_ashrrev_i32_e32 v3, 31, v2
	v_lshlrev_b64 v[4:5], 13, v[2:3]
	v_lshlrev_b64 v[2:3], 10, v[2:3]
	v_lshl_add_u64 v[18:19], v[102:103], 0, v[4:5]
	v_lshl_add_u64 v[62:63], v[104:105], 0, v[2:3]
	v_add_co_u32_e32 v64, vcc, s3, v18
	global_load_dwordx4 v[2:5], v[18:19], off nt
	global_load_dwordx4 v[6:9], v[18:19], off offset:1024 nt
	global_load_dwordx4 v[10:13], v[18:19], off offset:2048 nt
	global_load_dwordx4 v[14:17], v[18:19], off offset:3072 nt
	v_addc_co_u32_e32 v65, vcc, 0, v19, vcc
	global_load_dwordx4 v[34:37], v[62:63], off nt
	global_load_dwordx4 v[18:21], v[64:65], off nt
	global_load_dwordx4 v[22:25], v[64:65], off offset:1024 nt
	global_load_dwordx4 v[26:29], v[64:65], off offset:2048 nt
	global_load_dwordx4 v[30:33], v[64:65], off offset:3072 nt
	s_waitcnt lgkmcnt(13)
	v_add_f32_e32 v67, v68, v66
	v_mul_f32_e32 v184, 0xc3000000, v67
	s_waitcnt lgkmcnt(12)
	v_cvt_f32_ubyte3_e32 v169, v70
	v_cvt_f32_ubyte2_e32 v168, v70
	v_cvt_f32_ubyte1_e32 v171, v70
	v_cvt_f32_ubyte0_e32 v170, v70
	ds_read_b128 v[62:65], v123
	ds_read_b128 v[86:89], v123 offset:64
	ds_read_b128 v[90:93], v112
	ds_read_b128 v[136:139], v112 offset:4608
	ds_read_b128 v[140:143], v112 offset:9216
	ds_read_b128 v[144:147], v112 offset:13824
	ds_read_b128 v[148:151], v112 offset:18432
	ds_read_b128 v[152:155], v112 offset:23040
	ds_read_b128 v[156:159], v112 offset:27648
	ds_read_b128 v[160:163], v112 offset:32256
	s_waitcnt lgkmcnt(14)
	v_cvt_f32_ubyte1_e32 v165, v78
	v_cvt_f32_ubyte0_e32 v164, v78
	v_cvt_f32_ubyte3_e32 v167, v78
	v_cvt_f32_ubyte2_e32 v166, v78
	v_pk_fma_f32 v[170:171], v[170:171], v[68:69], v[184:185] op_sel_hi:[1,0,0]
	v_pk_fma_f32 v[168:169], v[168:169], v[68:69], v[184:185] op_sel_hi:[1,0,0]
	v_pk_fma_f32 v[164:165], v[164:165], v[66:67], v[170:171] op_sel_hi:[1,0,1]
	v_pk_fma_f32 v[166:167], v[166:167], v[66:67], v[168:169] op_sel_hi:[1,0,1]
	v_cvt_f32_ubyte1_e32 v169, v79
	v_cvt_f32_ubyte0_e32 v168, v79
	v_cvt_f32_ubyte3_e32 v171, v79
	v_cvt_f32_ubyte2_e32 v170, v79
	v_cvt_f32_ubyte3_e32 v79, v71
	v_cvt_f32_ubyte2_e32 v78, v71
	v_cvt_f32_ubyte1_e32 v173, v71
	v_cvt_f32_ubyte0_e32 v172, v71
	v_pk_fma_f32 v[70:71], v[172:173], v[68:69], v[184:185] op_sel_hi:[1,0,0]
	v_pk_fma_f32 v[78:79], v[78:79], v[68:69], v[184:185] op_sel_hi:[1,0,0]
	v_cvt_f32_ubyte3_e32 v173, v72
	v_cvt_f32_ubyte2_e32 v172, v72
	v_cvt_f32_ubyte1_e32 v175, v72
	v_cvt_f32_ubyte0_e32 v174, v72
	v_pk_fma_f32 v[170:171], v[170:171], v[66:67], v[78:79] op_sel_hi:[1,0,1]
	v_pk_fma_f32 v[168:169], v[168:169], v[66:67], v[70:71] op_sel_hi:[1,0,1]
	v_cvt_f32_ubyte1_e32 v71, v80
	v_cvt_f32_ubyte0_e32 v70, v80
	v_cvt_f32_ubyte3_e32 v79, v80
	v_cvt_f32_ubyte2_e32 v78, v80
	v_pk_fma_f32 v[176:177], v[174:175], v[68:69], v[184:185] op_sel_hi:[1,0,0]
	v_pk_fma_f32 v[172:173], v[172:173], v[68:69], v[184:185] op_sel_hi:[1,0,0]
	v_cvt_f32_ubyte2_e32 v80, v73
	v_pk_fma_f32 v[174:175], v[78:79], v[66:67], v[172:173] op_sel_hi:[1,0,1]
	v_pk_fma_f32 v[172:173], v[70:71], v[66:67], v[176:177] op_sel_hi:[1,0,1]
	v_cvt_f32_ubyte1_e32 v177, v73
	v_cvt_f32_ubyte0_e32 v176, v73
	v_cvt_f32_ubyte1_e32 v71, v81
	v_cvt_f32_ubyte0_e32 v70, v81
	v_cvt_f32_ubyte3_e32 v79, v81
	v_cvt_f32_ubyte2_e32 v78, v81
	v_cvt_f32_ubyte3_e32 v81, v73
	v_pk_fma_f32 v[176:177], v[176:177], v[68:69], v[184:185] op_sel_hi:[1,0,0]
	v_pk_fma_f32 v[72:73], v[80:81], v[68:69], v[184:185] op_sel_hi:[1,0,0]
	v_pk_fma_f32 v[70:71], v[70:71], v[66:67], v[176:177] op_sel_hi:[1,0,1]
	v_cvt_f32_ubyte3_e32 v177, v74
	v_cvt_f32_ubyte2_e32 v176, v74
	v_cvt_f32_ubyte1_e32 v179, v74
	v_cvt_f32_ubyte0_e32 v178, v74
	v_pk_fma_f32 v[72:73], v[78:79], v[66:67], v[72:73] op_sel_hi:[1,0,1]
	v_cvt_f32_ubyte1_e32 v79, v82
	v_cvt_f32_ubyte0_e32 v78, v82
	v_cvt_f32_ubyte3_e32 v81, v82
	v_cvt_f32_ubyte2_e32 v80, v82
	v_pk_fma_f32 v[178:179], v[178:179], v[68:69], v[184:185] op_sel_hi:[1,0,0]
	v_pk_fma_f32 v[176:177], v[176:177], v[68:69], v[184:185] op_sel_hi:[1,0,0]
	v_pk_fma_f32 v[78:79], v[78:79], v[66:67], v[178:179] op_sel_hi:[1,0,1]
	v_pk_fma_f32 v[80:81], v[80:81], v[66:67], v[176:177] op_sel_hi:[1,0,1]
	v_cvt_f32_ubyte1_e32 v177, v83
	v_cvt_f32_ubyte0_e32 v176, v83
	v_cvt_f32_ubyte3_e32 v179, v83
	v_cvt_f32_ubyte2_e32 v178, v83
	v_cvt_f32_ubyte3_e32 v83, v75
	v_cvt_f32_ubyte2_e32 v82, v75
	v_cvt_f32_ubyte1_e32 v181, v75
	v_cvt_f32_ubyte0_e32 v180, v75
	v_pk_fma_f32 v[74:75], v[180:181], v[68:69], v[184:185] op_sel_hi:[1,0,0]
	v_pk_fma_f32 v[82:83], v[82:83], v[68:69], v[184:185] op_sel_hi:[1,0,0]
	v_cvt_f32_ubyte3_e32 v181, v76
	v_cvt_f32_ubyte2_e32 v180, v76
	v_cvt_f32_ubyte1_e32 v183, v76
	v_cvt_f32_ubyte0_e32 v182, v76
	v_pk_fma_f32 v[178:179], v[178:179], v[66:67], v[82:83] op_sel_hi:[1,0,1]
	v_pk_fma_f32 v[176:177], v[176:177], v[66:67], v[74:75] op_sel_hi:[1,0,1]
	v_cvt_f32_ubyte1_e32 v75, v84
	v_cvt_f32_ubyte0_e32 v74, v84
	v_cvt_f32_ubyte3_e32 v83, v84
	v_cvt_f32_ubyte2_e32 v82, v84
	v_pk_fma_f32 v[186:187], v[182:183], v[68:69], v[184:185] op_sel_hi:[1,0,0]
	v_pk_fma_f32 v[180:181], v[180:181], v[68:69], v[184:185] op_sel_hi:[1,0,0]
	v_cvt_f32_ubyte2_e32 v84, v77
	v_pk_fma_f32 v[182:183], v[82:83], v[66:67], v[180:181] op_sel_hi:[1,0,1]
	v_pk_fma_f32 v[180:181], v[74:75], v[66:67], v[186:187] op_sel_hi:[1,0,1]
	v_cvt_f32_ubyte1_e32 v75, v85
	v_cvt_f32_ubyte0_e32 v74, v85
	v_cvt_f32_ubyte3_e32 v83, v85
	v_cvt_f32_ubyte2_e32 v82, v85
	v_cvt_f32_ubyte3_e32 v85, v77
	v_cvt_f32_ubyte1_e32 v187, v77
	v_cvt_f32_ubyte0_e32 v186, v77
	v_pk_fma_f32 v[76:77], v[186:187], v[68:69], v[184:185] op_sel_hi:[1,0,0]
	v_pk_fma_f32 v[68:69], v[84:85], v[68:69], v[184:185] op_sel_hi:[1,0,0]
	s_nop 0
	v_pk_fma_f32 v[68:69], v[82:83], v[66:67], v[68:69] op_sel_hi:[1,0,1]
	v_pk_fma_f32 v[66:67], v[74:75], v[66:67], v[76:77] op_sel_hi:[1,0,1]
	ds_read_b128 v[74:77], v123 offset:128
	ds_read_b128 v[82:85], v123 offset:192
	ds_read_b128 v[184:187], v112 offset:64
	ds_read_b128 v[188:191], v112 offset:4672
	ds_read_b128 v[192:195], v112 offset:9280
	ds_read_b128 v[196:199], v112 offset:13888
	ds_read_b128 v[200:203], v112 offset:18496
	ds_read_b128 v[204:207], v112 offset:23104
	ds_read_b128 v[208:211], v112 offset:27712
	ds_read_b128 v[212:215], v112 offset:32320
	s_waitcnt lgkmcnt(14)
	v_cvt_pk_bf16_f32 v62, v62, v63
	v_cvt_pk_bf16_f32 v63, v64, v65
	v_cvt_pk_bf16_f32 v64, v86, v87
	v_cvt_pk_bf16_f32 v65, v88, v89
	s_nop 1
	v_mfma_f32_16x16x32_bf16 v[86:89], v[90:93], v[62:65], v[164:167]
	v_mfma_f32_16x16x32_bf16 v[90:93], v[136:139], v[62:65], v[168:171]
	v_mfma_f32_16x16x32_bf16 v[136:139], v[140:143], v[62:65], v[172:175]
	v_mfma_f32_16x16x32_bf16 v[70:73], v[144:147], v[62:65], v[70:73]
	s_waitcnt lgkmcnt(13)
	v_mfma_f32_16x16x32_bf16 v[78:81], v[148:151], v[62:65], v[78:81]
	s_waitcnt lgkmcnt(12)
	v_mfma_f32_16x16x32_bf16 v[140:143], v[152:155], v[62:65], v[176:179]
	s_waitcnt lgkmcnt(11)
	v_mfma_f32_16x16x32_bf16 v[144:147], v[156:159], v[62:65], v[180:183]
	s_waitcnt lgkmcnt(10)
	v_mfma_f32_16x16x32_bf16 v[62:65], v[160:163], v[62:65], v[66:69]
	s_nop 2
	ds_read_b128 v[66:69], v123 offset:256
	ds_read_b128 v[148:151], v123 offset:320
	ds_read_b128 v[152:155], v112 offset:128
	ds_read_b128 v[156:159], v112 offset:4736
	ds_read_b128 v[160:163], v112 offset:9344
	ds_read_b128 v[164:167], v112 offset:13952
	ds_read_b128 v[168:171], v112 offset:18560
	ds_read_b128 v[172:175], v112 offset:23168
	ds_read_b128 v[176:179], v112 offset:27776
	ds_read_b128 v[180:183], v112 offset:32384
	s_waitcnt lgkmcnt(14)
	v_cvt_pk_bf16_f32 v74, v74, v75
	v_cvt_pk_bf16_f32 v75, v76, v77
	v_cvt_pk_bf16_f32 v76, v82, v83
	v_cvt_pk_bf16_f32 v77, v84, v85
	s_waitcnt lgkmcnt(10)
	s_nop 0
	v_mfma_f32_16x16x32_bf16 v[62:65], v[212:215], v[74:77], v[62:65]
	v_mfma_f32_16x16x32_bf16 v[82:85], v[184:187], v[74:77], v[86:89]
	v_mfma_f32_16x16x32_bf16 v[86:89], v[188:191], v[74:77], v[90:93]
	v_mfma_f32_16x16x32_bf16 v[90:93], v[192:195], v[74:77], v[136:139]
	v_mfma_f32_16x16x32_bf16 v[70:73], v[196:199], v[74:77], v[70:73]
	v_mfma_f32_16x16x32_bf16 v[78:81], v[200:203], v[74:77], v[78:81]
	v_mfma_f32_16x16x32_bf16 v[136:139], v[204:207], v[74:77], v[140:143]
	v_mfma_f32_16x16x32_bf16 v[140:143], v[208:211], v[74:77], v[144:147]
	ds_read_b128 v[74:77], v123 offset:384
	s_nop 1
	ds_read_b128 v[144:147], v123 offset:448
	ds_read_b128 v[184:187], v112 offset:192
	ds_read_b128 v[188:191], v112 offset:4800
	ds_read_b128 v[192:195], v112 offset:9408
	ds_read_b128 v[196:199], v112 offset:14016
	ds_read_b128 v[200:203], v112 offset:18624
	ds_read_b128 v[204:207], v112 offset:23232
	ds_read_b128 v[208:211], v112 offset:27840
	ds_read_b128 v[212:215], v112 offset:32448
	s_waitcnt lgkmcnt(14)
	v_cvt_pk_bf16_f32 v66, v66, v67
	v_cvt_pk_bf16_f32 v67, v68, v69
	v_cvt_pk_bf16_f32 v68, v148, v149
	v_cvt_pk_bf16_f32 v69, v150, v151
	s_waitcnt lgkmcnt(10)
	s_nop 0
	v_mfma_f32_16x16x32_bf16 v[62:65], v[180:183], v[66:69], v[62:65]
	v_mfma_f32_16x16x32_bf16 v[82:85], v[152:155], v[66:69], v[82:85]
	v_mfma_f32_16x16x32_bf16 v[86:89], v[156:159], v[66:69], v[86:89]
	v_mfma_f32_16x16x32_bf16 v[90:93], v[160:163], v[66:69], v[90:93]
	v_mfma_f32_16x16x32_bf16 v[70:73], v[164:167], v[66:69], v[70:73]
	v_mfma_f32_16x16x32_bf16 v[78:81], v[168:171], v[66:69], v[78:81]
	v_mfma_f32_16x16x32_bf16 v[136:139], v[172:175], v[66:69], v[136:139]
	v_mfma_f32_16x16x32_bf16 v[140:143], v[176:179], v[66:69], v[140:143]
	ds_read2st64_b64 v[66:69], v134 offset0:54 offset1:63
	ds_read2st64_b64 v[148:151], v134 offset0:36 offset1:45
	ds_read2st64_b64 v[152:155], v134 offset0:18 offset1:27
	ds_read2st64_b64 v[156:159], v134 offset1:9
	ds_read_b128 v[160:163], v124 offset:8704
	s_waitcnt lgkmcnt(14)
	v_cvt_pk_bf16_f32 v74, v74, v75
	v_cvt_pk_bf16_f32 v75, v76, v77
	s_waitcnt lgkmcnt(13)
	v_cvt_pk_bf16_f32 v76, v144, v145
	v_cvt_pk_bf16_f32 v77, v146, v147
	s_waitcnt lgkmcnt(5)
	s_nop 0
	v_mfma_f32_16x16x32_bf16 v[62:65], v[212:215], v[74:77], v[62:65]
	v_mfma_f32_16x16x32_bf16 v[82:85], v[184:187], v[74:77], v[82:85]
	v_mfma_f32_16x16x32_bf16 v[86:89], v[188:191], v[74:77], v[86:89]
	v_mfma_f32_16x16x32_bf16 v[90:93], v[192:195], v[74:77], v[90:93]
	v_mfma_f32_16x16x32_bf16 v[70:73], v[196:199], v[74:77], v[70:73]
	v_mfma_f32_16x16x32_bf16 v[78:81], v[200:203], v[74:77], v[78:81]
	v_mfma_f32_16x16x32_bf16 v[136:139], v[204:207], v[74:77], v[136:139]
	v_mfma_f32_16x16x32_bf16 v[140:143], v[208:211], v[74:77], v[140:143]
	ds_read_b128 v[144:147], v125
	ds_read_b128 v[164:167], v126
	ds_read_b128 v[168:171], v127
	ds_read_b128 v[172:175], v128
	ds_read_b128 v[176:179], v129
	ds_read_b128 v[180:183], v130
	ds_read_b128 v[184:187], v131
	ds_read_b128 v[188:191], v132
	ds_read_b128 v[192:195], v112 offset:36864
	ds_read_b128 v[196:199], v112 offset:41472
	ds_read_b128 v[200:203], v112 offset:46080
	ds_read_b128 v[204:207], v112 offset:50688
	ds_read_b128 v[208:211], v112 offset:55296
	ds_read_b128 v[212:215], v112 offset:59904
	ds_read_b128 v[216:219], v112 offset:64512
	ds_read_b128 v[220:223], v113 offset:32256
	s_waitcnt lgkmcnt(14)
	v_cvt_pk_bf16_f32 v74, v160, v161
	v_cvt_pk_bf16_f32 v75, v162, v163
	s_nop 1
	v_mfma_f32_16x16x16_bf16 v[160:163], v[156:157], v[74:75], v[82:85]
	v_mfma_f32_16x16x16_bf16 v[86:89], v[158:159], v[74:75], v[86:89]
	v_mfma_f32_16x16x16_bf16 v[90:93], v[152:153], v[74:75], v[90:93]
	v_mfma_f32_16x16x16_bf16 v[70:73], v[154:155], v[74:75], v[70:73]
	v_mfma_f32_16x16x16_bf16 v[78:81], v[148:149], v[74:75], v[78:81]
	v_mfma_f32_16x16x16_bf16 v[136:139], v[150:151], v[74:75], v[136:139]
	v_mfma_f32_16x16x16_bf16 v[82:85], v[66:67], v[74:75], v[140:143]
	v_mfma_f32_16x16x16_bf16 v[74:77], v[68:69], v[74:75], v[62:65]
	s_nop 2
	v_exp_f32_e32 v62, v160
	v_exp_f32_e32 v63, v161
	v_exp_f32_e32 v64, v162
	v_exp_f32_e32 v65, v163
	v_add_f32_e32 v62, 1.0, v62
	v_add_f32_e32 v63, 1.0, v63
	v_rcp_f32_e32 v62, v62
	v_rcp_f32_e32 v63, v63
	v_add_f32_e32 v64, 1.0, v64
	v_add_f32_e32 v65, 1.0, v65
	v_rcp_f32_e32 v64, v64
	v_rcp_f32_e32 v65, v65
	v_pk_mul_f32 v[62:63], v[160:161], v[62:63]
	v_exp_f32_e32 v66, v86
	v_cvt_pk_bf16_f32 v140, v62, v63
	v_pk_mul_f32 v[62:63], v[162:163], v[64:65]
	v_exp_f32_e32 v64, v88
	v_cvt_pk_bf16_f32 v141, v62, v63
	v_exp_f32_e32 v63, v87
	v_exp_f32_e32 v65, v89
	v_add_f32_e32 v62, 1.0, v66
	v_rcp_f32_e32 v62, v62
	v_add_f32_e32 v63, 1.0, v63
	v_rcp_f32_e32 v63, v63
	v_add_f32_e32 v64, 1.0, v64
	v_add_f32_e32 v65, 1.0, v65
	v_rcp_f32_e32 v64, v64
	v_rcp_f32_e32 v65, v65
	v_pk_mul_f32 v[62:63], v[86:87], v[62:63]
	v_exp_f32_e32 v66, v90
	v_cvt_pk_bf16_f32 v142, v62, v63
	v_pk_mul_f32 v[62:63], v[88:89], v[64:65]
	v_exp_f32_e32 v64, v92
	v_cvt_pk_bf16_f32 v143, v62, v63
	v_exp_f32_e32 v63, v91
	v_exp_f32_e32 v65, v93
	v_add_f32_e32 v62, 1.0, v66
	v_rcp_f32_e32 v62, v62
	v_add_f32_e32 v63, 1.0, v63
	v_rcp_f32_e32 v63, v63
	v_add_f32_e32 v64, 1.0, v64
	v_add_f32_e32 v65, 1.0, v65
	v_rcp_f32_e32 v64, v64
	v_rcp_f32_e32 v65, v65
	v_pk_mul_f32 v[62:63], v[90:91], v[62:63]
	v_exp_f32_e32 v66, v70
	v_cvt_pk_bf16_f32 v86, v62, v63
	v_pk_mul_f32 v[62:63], v[92:93], v[64:65]
	v_exp_f32_e32 v64, v72
	v_cvt_pk_bf16_f32 v87, v62, v63
	v_exp_f32_e32 v63, v71
	v_exp_f32_e32 v65, v73
	v_add_f32_e32 v62, 1.0, v66
	v_rcp_f32_e32 v62, v62
	v_add_f32_e32 v63, 1.0, v63
	v_rcp_f32_e32 v63, v63
	v_add_f32_e32 v64, 1.0, v64
	v_add_f32_e32 v65, 1.0, v65
	v_rcp_f32_e32 v64, v64
	v_rcp_f32_e32 v65, v65
	v_pk_mul_f32 v[62:63], v[70:71], v[62:63]
	v_exp_f32_e32 v66, v78
	v_cvt_pk_bf16_f32 v88, v62, v63
	v_pk_mul_f32 v[62:63], v[72:73], v[64:65]
	v_exp_f32_e32 v64, v80
	v_cvt_pk_bf16_f32 v89, v62, v63
	v_exp_f32_e32 v63, v79
	v_exp_f32_e32 v65, v81
	v_add_f32_e32 v62, 1.0, v66
	v_rcp_f32_e32 v62, v62
	v_add_f32_e32 v63, 1.0, v63
	v_rcp_f32_e32 v63, v63
	v_add_f32_e32 v64, 1.0, v64
	v_add_f32_e32 v65, 1.0, v65
	v_rcp_f32_e32 v64, v64
	v_rcp_f32_e32 v65, v65
	v_exp_f32_e32 v66, v136
	v_pk_mul_f32 v[62:63], v[78:79], v[62:63]
	v_exp_f32_e32 v67, v139
	v_cvt_pk_bf16_f32 v148, v62, v63
	v_pk_mul_f32 v[62:63], v[80:81], v[64:65]
	v_exp_f32_e32 v65, v137
	v_add_f32_e32 v64, 1.0, v66
	v_exp_f32_e32 v66, v138
	v_rcp_f32_e32 v64, v64
	v_add_f32_e32 v65, 1.0, v65
	v_rcp_f32_e32 v65, v65
	v_add_f32_e32 v66, 1.0, v66
	v_add_f32_e32 v67, 1.0, v67
	v_rcp_f32_e32 v66, v66
	v_rcp_f32_e32 v67, v67
	v_cvt_pk_bf16_f32 v149, v62, v63
	v_pk_mul_f32 v[62:63], v[136:137], v[64:65]
	s_nop 0
	v_cvt_pk_bf16_f32 v150, v62, v63
	v_pk_mul_f32 v[62:63], v[138:139], v[66:67]
	s_nop 0
	v_cvt_pk_bf16_f32 v151, v62, v63
	ds_read_b128 v[90:93], v112 offset:36928
	ds_read_b128 v[136:139], v112 offset:41536
	ds_read_b128 v[152:155], v112 offset:46144
	ds_read_b128 v[156:159], v112 offset:50752
	ds_read_b128 v[160:163], v112 offset:55360
	ds_read_b128 v[224:227], v112 offset:59968
	ds_read_b128 v[228:231], v112 offset:64576
	ds_read_b128 v[232:235], v113 offset:32320
	ds_read_b128 v[62:65], v123
	ds_read_b128 v[66:69], v123 offset:64
	s_waitcnt lgkmcnt(14)
	v_mfma_f32_16x16x32_bf16 v[144:147], v[192:195], v[140:143], v[144:147]
	v_mfma_f32_16x16x32_bf16 v[164:167], v[196:199], v[140:143], v[164:167]
	v_mfma_f32_16x16x32_bf16 v[168:171], v[200:203], v[140:143], v[168:171]
	v_mfma_f32_16x16x32_bf16 v[172:175], v[204:207], v[140:143], v[172:175]
	s_waitcnt lgkmcnt(13)
	v_mfma_f32_16x16x32_bf16 v[176:179], v[208:211], v[140:143], v[176:179]
	s_waitcnt lgkmcnt(12)
	v_mfma_f32_16x16x32_bf16 v[180:183], v[212:215], v[140:143], v[180:183]
	s_waitcnt lgkmcnt(11)
	v_mfma_f32_16x16x32_bf16 v[184:187], v[216:219], v[140:143], v[184:187]
	s_waitcnt lgkmcnt(10)
	v_mfma_f32_16x16x32_bf16 v[140:143], v[220:223], v[140:143], v[188:191]
	s_nop 2
	ds_read_b128 v[188:191], v112 offset:36992
	ds_read_b128 v[192:195], v112 offset:41600
	ds_read_b128 v[196:199], v112 offset:46208
	ds_read_b128 v[200:203], v112 offset:50816
	ds_read_b128 v[204:207], v112 offset:55424
	ds_read_b128 v[208:211], v112 offset:60032
	ds_read_b128 v[212:215], v112 offset:64640
	ds_read_b128 v[216:219], v113 offset:32384
	ds_read_b128 v[70:73], v123 offset:128
	ds_read_b128 v[78:81], v123 offset:192
	s_waitcnt lgkmcnt(14)
	v_mfma_f32_16x16x32_bf16 v[144:147], v[90:93], v[86:89], v[144:147]
	v_mfma_f32_16x16x32_bf16 v[136:139], v[136:139], v[86:89], v[164:167]
	v_mfma_f32_16x16x32_bf16 v[152:155], v[152:155], v[86:89], v[168:171]
	v_mfma_f32_16x16x32_bf16 v[156:159], v[156:159], v[86:89], v[172:175]
	v_mfma_f32_16x16x32_bf16 v[160:163], v[160:163], v[86:89], v[176:179]
	v_mfma_f32_16x16x32_bf16 v[164:167], v[224:227], v[86:89], v[180:183]
	s_waitcnt lgkmcnt(13)
	v_mfma_f32_16x16x32_bf16 v[168:171], v[228:231], v[86:89], v[184:187]
	s_waitcnt lgkmcnt(12)
	v_mfma_f32_16x16x32_bf16 v[140:143], v[232:235], v[86:89], v[140:143]
	ds_read_b128 v[172:175], v112 offset:37056
	ds_read_b128 v[176:179], v112 offset:41664
	ds_read_b128 v[180:183], v112 offset:46272
	ds_read_b128 v[184:187], v112 offset:50880
	ds_read_b128 v[220:223], v112 offset:55488
	ds_read_b128 v[224:227], v112 offset:60096
	ds_read_b128 v[228:231], v112 offset:64704
	ds_read_b128 v[232:235], v113 offset:32448
	ds_read_b128 v[86:89], v123 offset:256
	ds_read_b128 v[90:93], v123 offset:320
	s_waitcnt lgkmcnt(14)
	v_mfma_f32_16x16x32_bf16 v[144:147], v[188:191], v[148:151], v[144:147]
	v_mfma_f32_16x16x32_bf16 v[136:139], v[192:195], v[148:151], v[136:139]
	v_mfma_f32_16x16x32_bf16 v[152:155], v[196:199], v[148:151], v[152:155]
	v_mfma_f32_16x16x32_bf16 v[156:159], v[200:203], v[148:151], v[156:159]
	v_mfma_f32_16x16x32_bf16 v[160:163], v[204:207], v[148:151], v[160:163]
	v_mfma_f32_16x16x32_bf16 v[164:167], v[208:211], v[148:151], v[164:167]
	s_waitcnt lgkmcnt(13)
	v_mfma_f32_16x16x32_bf16 v[168:171], v[212:215], v[148:151], v[168:171]
	s_waitcnt lgkmcnt(12)
	v_mfma_f32_16x16x32_bf16 v[140:143], v[216:219], v[148:151], v[140:143]
	v_exp_f32_e32 v148, v82
	v_exp_f32_e32 v149, v83
	v_exp_f32_e32 v150, v84
	v_exp_f32_e32 v151, v85
	v_add_f32_e32 v148, 1.0, v148
	v_add_f32_e32 v149, 1.0, v149
	v_rcp_f32_e32 v148, v148
	v_rcp_f32_e32 v149, v149
	v_add_f32_e32 v150, 1.0, v150
	v_add_f32_e32 v151, 1.0, v151
	v_rcp_f32_e32 v150, v150
	v_rcp_f32_e32 v151, v151
	v_pk_mul_f32 v[82:83], v[82:83], v[148:149]
	v_exp_f32_e32 v148, v74
	v_cvt_pk_bf16_f32 v82, v82, v83
	v_pk_mul_f32 v[84:85], v[84:85], v[150:151]
	v_exp_f32_e32 v149, v77
	v_cvt_pk_bf16_f32 v83, v84, v85
	v_exp_f32_e32 v85, v75
	v_add_f32_e32 v84, 1.0, v148
	v_exp_f32_e32 v148, v76
	v_rcp_f32_e32 v84, v84
	v_add_f32_e32 v85, 1.0, v85
	v_rcp_f32_e32 v85, v85
	v_add_f32_e32 v148, 1.0, v148
	v_rcp_f32_e32 v192, v148
	v_add_f32_e32 v148, 1.0, v149
	v_rcp_f32_e32 v193, v148
	ds_read_b128 v[148:151], v123 offset:384
	ds_read_b128 v[188:191], v123 offset:448
	v_pk_mul_f32 v[74:75], v[74:75], v[84:85]
	s_nop 0
	v_cvt_pk_bf16_f32 v84, v74, v75
	v_pk_mul_f32 v[74:75], v[76:77], v[192:193]
	s_nop 0
	v_cvt_pk_bf16_f32 v85, v74, v75
	s_waitcnt lgkmcnt(11)
	s_nop 0
	v_mfma_f32_16x16x32_bf16 v[74:77], v[172:175], v[82:85], v[144:147]
	s_waitcnt lgkmcnt(10)
	v_mfma_f32_16x16x32_bf16 v[136:139], v[176:179], v[82:85], v[136:139]
	s_waitcnt lgkmcnt(9)
	v_mfma_f32_16x16x32_bf16 v[144:147], v[180:183], v[82:85], v[152:155]
	s_waitcnt lgkmcnt(8)
	v_mfma_f32_16x16x32_bf16 v[152:155], v[184:187], v[82:85], v[156:159]
	s_waitcnt lgkmcnt(7)
	v_mfma_f32_16x16x32_bf16 v[156:159], v[220:223], v[82:85], v[160:163]
	s_waitcnt lgkmcnt(6)
	v_mfma_f32_16x16x32_bf16 v[160:163], v[224:227], v[82:85], v[164:167]
	s_waitcnt lgkmcnt(5)
	v_mfma_f32_16x16x32_bf16 v[164:167], v[228:231], v[82:85], v[168:171]
	s_waitcnt lgkmcnt(4)
	v_mfma_f32_16x16x32_bf16 v[82:85], v[232:235], v[82:85], v[140:143]
	s_nop 2
	v_exp_f32_e32 v140, v74
	v_exp_f32_e32 v141, v75
	v_exp_f32_e32 v168, v136
	v_exp_f32_e32 v169, v137
	v_exp_f32_e32 v170, v138
	v_exp_f32_e32 v171, v139
	v_exp_f32_e32 v142, v76
	v_exp_f32_e32 v143, v77
	v_add_f32_e32 v140, 1.0, v140
	v_add_f32_e32 v141, 1.0, v141
	v_rcp_f32_e32 v140, v140
	v_rcp_f32_e32 v141, v141
	v_add_f32_e32 v168, 1.0, v168
	v_add_f32_e32 v169, 1.0, v169
	v_rcp_f32_e32 v168, v168
	v_rcp_f32_e32 v169, v169
	v_add_f32_e32 v170, 1.0, v170
	v_add_f32_e32 v171, 1.0, v171
	v_add_f32_e32 v142, 1.0, v142
	v_add_f32_e32 v143, 1.0, v143
	v_rcp_f32_e32 v170, v170
	v_rcp_f32_e32 v171, v171
	v_rcp_f32_e32 v142, v142
	v_rcp_f32_e32 v143, v143
	v_exp_f32_e32 v172, v144
	v_exp_f32_e32 v173, v145
	v_pk_mul_f32 v[74:75], v[74:75], v[140:141]
	v_pk_mul_f32 v[136:137], v[136:137], v[168:169]
	v_pk_fma_f32 v[62:63], v[74:75], s[2:3], v[62:63] op_sel_hi:[1,0,1]
	v_exp_f32_e32 v174, v146
	v_pk_mul_f32 v[236:237], v[62:63], v[62:63]
	v_exp_f32_e32 v175, v147
	v_pk_fma_f32 v[66:67], v[136:137], s[2:3], v[66:67] op_sel_hi:[1,0,1]
	v_pk_mul_f32 v[136:137], v[138:139], v[170:171]
	v_pk_fma_f32 v[236:237], v[66:67], v[66:67], v[236:237]
	v_add_f32_e32 v74, 0, v62
	v_pk_fma_f32 v[68:69], v[136:137], s[2:3], v[68:69] op_sel_hi:[1,0,1]
	v_add_f32_e32 v136, v63, v74
	v_pk_fma_f32 v[236:237], v[68:69], v[68:69], v[236:237]
	v_pk_mul_f32 v[74:75], v[76:77], v[142:143]
	v_add_f32_e32 v172, 1.0, v172
	v_add_f32_e32 v173, 1.0, v173
	v_exp_f32_e32 v176, v152
	v_exp_f32_e32 v177, v153
	v_pk_fma_f32 v[64:65], v[74:75], s[2:3], v[64:65] op_sel_hi:[1,0,1]
	v_rcp_f32_e32 v172, v172
	v_pk_fma_f32 v[236:237], v[64:65], v[64:65], v[236:237]
	v_rcp_f32_e32 v173, v173
	v_add_f32_e32 v74, v64, v136
	v_add_f32_e32 v174, 1.0, v174
	v_add_f32_e32 v175, 1.0, v175
	v_exp_f32_e32 v178, v154
	v_exp_f32_e32 v179, v155
	v_add_f32_e32 v74, v65, v74
	v_rcp_f32_e32 v174, v174
	v_rcp_f32_e32 v175, v175
	v_add_f32_e32 v74, v66, v74
	v_add_f32_e32 v176, 1.0, v176
	v_add_f32_e32 v177, 1.0, v177
	v_exp_f32_e32 v180, v156
	v_exp_f32_e32 v181, v157
	v_add_f32_e32 v74, v67, v74
	v_rcp_f32_e32 v176, v176
	v_rcp_f32_e32 v177, v177
	v_pk_mul_f32 v[144:145], v[144:145], v[172:173]
	v_add_f32_e32 v74, v68, v74
	v_add_f32_e32 v178, 1.0, v178
	v_add_f32_e32 v179, 1.0, v179
	v_exp_f32_e32 v182, v158
	v_exp_f32_e32 v183, v159
	v_pk_fma_f32 v[70:71], v[144:145], s[2:3], v[70:71] op_sel_hi:[1,0,1]
	v_add_f32_e32 v74, v69, v74
	v_pk_fma_f32 v[236:237], v[70:71], v[70:71], v[236:237]
	v_rcp_f32_e32 v178, v178
	v_rcp_f32_e32 v179, v179
	v_pk_mul_f32 v[144:145], v[146:147], v[174:175]
	v_add_f32_e32 v74, v70, v74
	v_add_f32_e32 v180, 1.0, v180
	v_add_f32_e32 v181, 1.0, v181
	v_exp_f32_e32 v184, v160
	v_exp_f32_e32 v185, v161
	v_pk_fma_f32 v[72:73], v[144:145], s[2:3], v[72:73] op_sel_hi:[1,0,1]
	v_add_f32_e32 v74, v71, v74
	v_pk_fma_f32 v[236:237], v[72:73], v[72:73], v[236:237]
	v_rcp_f32_e32 v180, v180
	v_rcp_f32_e32 v181, v181
	v_pk_mul_f32 v[152:153], v[152:153], v[176:177]
	v_add_f32_e32 v74, v72, v74
	v_add_f32_e32 v182, 1.0, v182
	v_add_f32_e32 v183, 1.0, v183
	v_exp_f32_e32 v186, v162
	v_exp_f32_e32 v187, v163
	v_pk_fma_f32 v[78:79], v[152:153], s[2:3], v[78:79] op_sel_hi:[1,0,1]
	v_add_f32_e32 v74, v73, v74
	v_pk_fma_f32 v[236:237], v[78:79], v[78:79], v[236:237]
	v_rcp_f32_e32 v182, v182
	v_rcp_f32_e32 v183, v183
	v_pk_mul_f32 v[152:153], v[154:155], v[178:179]
	v_add_f32_e32 v74, v78, v74
	v_add_f32_e32 v184, 1.0, v184
	v_add_f32_e32 v185, 1.0, v185
	v_exp_f32_e32 v192, v164
	v_exp_f32_e32 v193, v165
	v_pk_fma_f32 v[80:81], v[152:153], s[2:3], v[80:81] op_sel_hi:[1,0,1]
	v_add_f32_e32 v74, v79, v74
	v_pk_fma_f32 v[236:237], v[80:81], v[80:81], v[236:237]
	v_rcp_f32_e32 v184, v184
	v_rcp_f32_e32 v185, v185
	v_pk_mul_f32 v[156:157], v[156:157], v[180:181]
	v_add_f32_e32 v74, v80, v74
	v_add_f32_e32 v186, 1.0, v186
	v_add_f32_e32 v187, 1.0, v187
	v_exp_f32_e32 v194, v166
	v_exp_f32_e32 v195, v167
	s_waitcnt lgkmcnt(3)
	v_pk_fma_f32 v[86:87], v[156:157], s[2:3], v[86:87] op_sel_hi:[1,0,1]
	v_add_f32_e32 v74, v81, v74
	v_pk_fma_f32 v[236:237], v[86:87], v[86:87], v[236:237]
	v_rcp_f32_e32 v186, v186
	v_rcp_f32_e32 v187, v187
	v_pk_mul_f32 v[156:157], v[158:159], v[182:183]
	v_add_f32_e32 v74, v86, v74
	v_add_f32_e32 v192, 1.0, v192
	v_add_f32_e32 v193, 1.0, v193
	v_exp_f32_e32 v196, v82
	v_exp_f32_e32 v197, v83
	v_pk_fma_f32 v[88:89], v[156:157], s[2:3], v[88:89] op_sel_hi:[1,0,1]
	v_add_f32_e32 v74, v87, v74
	v_pk_fma_f32 v[236:237], v[88:89], v[88:89], v[236:237]
	v_rcp_f32_e32 v192, v192
	v_rcp_f32_e32 v193, v193
	v_pk_mul_f32 v[160:161], v[160:161], v[184:185]
	v_add_f32_e32 v74, v88, v74
	v_add_f32_e32 v194, 1.0, v194
	v_add_f32_e32 v195, 1.0, v195
	v_exp_f32_e32 v198, v84
	v_exp_f32_e32 v199, v85
	s_waitcnt lgkmcnt(2)
	v_pk_fma_f32 v[90:91], v[160:161], s[2:3], v[90:91] op_sel_hi:[1,0,1]
	v_add_f32_e32 v74, v89, v74
	v_pk_fma_f32 v[236:237], v[90:91], v[90:91], v[236:237]
	v_rcp_f32_e32 v194, v194
	v_rcp_f32_e32 v195, v195
	v_pk_mul_f32 v[160:161], v[162:163], v[186:187]
	v_add_f32_e32 v74, v90, v74
	v_add_f32_e32 v196, 1.0, v196
	v_add_f32_e32 v197, 1.0, v197
	v_pk_fma_f32 v[92:93], v[160:161], s[2:3], v[92:93] op_sel_hi:[1,0,1]
	v_add_f32_e32 v74, v91, v74
	v_pk_fma_f32 v[236:237], v[92:93], v[92:93], v[236:237]
	v_rcp_f32_e32 v196, v196
	v_rcp_f32_e32 v197, v197
	v_pk_mul_f32 v[164:165], v[164:165], v[192:193]
	v_add_f32_e32 v74, v92, v74
	v_add_f32_e32 v198, 1.0, v198
	v_add_f32_e32 v199, 1.0, v199
	s_waitcnt lgkmcnt(1)
	v_pk_fma_f32 v[148:149], v[164:165], s[2:3], v[148:149] op_sel_hi:[1,0,1]
	v_add_f32_e32 v74, v93, v74
	v_pk_fma_f32 v[236:237], v[148:149], v[148:149], v[236:237]
	v_rcp_f32_e32 v198, v198
	v_rcp_f32_e32 v199, v199
	v_pk_mul_f32 v[164:165], v[166:167], v[194:195]
	v_add_f32_e32 v74, v148, v74
	v_pk_fma_f32 v[150:151], v[164:165], s[2:3], v[150:151] op_sel_hi:[1,0,1]
	v_add_f32_e32 v74, v149, v74
	v_pk_fma_f32 v[236:237], v[150:151], v[150:151], v[236:237]
	v_pk_mul_f32 v[82:83], v[82:83], v[196:197]
	v_add_f32_e32 v74, v150, v74
	s_waitcnt lgkmcnt(0)
	v_pk_fma_f32 v[82:83], v[82:83], s[2:3], v[188:189] op_sel_hi:[1,0,1]
	v_add_f32_e32 v74, v151, v74
	v_pk_fma_f32 v[236:237], v[82:83], v[82:83], v[236:237]
	v_pk_mul_f32 v[84:85], v[84:85], v[198:199]
	v_add_f32_e32 v74, v82, v74
	v_pk_fma_f32 v[84:85], v[84:85], s[2:3], v[190:191] op_sel_hi:[1,0,1]
	v_add_f32_e32 v74, v83, v74
	v_pk_fma_f32 v[236:237], v[84:85], v[84:85], v[236:237]
	v_add_f32_e32 v74, v84, v74
	v_add_f32_e32 v74, v85, v74
	v_add_f32_e32 v75, v236, v237
	s_nop 1
	v_permlane16_swap_b32_e32 v74, v75
	s_nop 0
	v_add_f32_e32 v74, v74, v75
	v_mov_b32_e32 v75, v74
	s_nop 1
	v_permlane32_swap_b32_e32 v74, v75
	s_nop 0
	v_add_f32_e32 v74, v74, v75
	v_mov_b32_e32 v75, v74
	s_nop 1
	v_permlane16_swap_b32_e32 v74, v75
	s_nop 0
	v_mul_f32_e32 v74, 0x3c000000, v74
	v_mul_f32_e32 v75, 0x3c000000, v75
	v_fma_f32 v75, -v74, v74, v75
	v_add_f32_e32 v75, 0x3727c5ac, v75
	v_rsq_f32_e32 v76, v75
	s_nop 0
	v_mul_f32_e64 v236, -v74, v76
	v_pk_fma_f32 v[62:63], v[62:63], v[76:77], v[236:237] op_sel_hi:[1,0,0]
	v_pk_fma_f32 v[64:65], v[64:65], v[76:77], v[236:237] op_sel_hi:[1,0,0]
	v_pk_fma_f32 v[66:67], v[66:67], v[76:77], v[236:237] op_sel_hi:[1,0,0]
	v_pk_fma_f32 v[68:69], v[68:69], v[76:77], v[236:237] op_sel_hi:[1,0,0]
	ds_write_b128 v123, v[62:65]
	v_pk_fma_f32 v[70:71], v[70:71], v[76:77], v[236:237] op_sel_hi:[1,0,0]
	v_pk_fma_f32 v[72:73], v[72:73], v[76:77], v[236:237] op_sel_hi:[1,0,0]
	ds_write_b128 v123, v[66:69] offset:64
	v_pk_fma_f32 v[78:79], v[78:79], v[76:77], v[236:237] op_sel_hi:[1,0,0]
	v_pk_fma_f32 v[80:81], v[80:81], v[76:77], v[236:237] op_sel_hi:[1,0,0]
	ds_write_b128 v123, v[70:73] offset:128
	v_pk_fma_f32 v[86:87], v[86:87], v[76:77], v[236:237] op_sel_hi:[1,0,0]
	v_pk_fma_f32 v[88:89], v[88:89], v[76:77], v[236:237] op_sel_hi:[1,0,0]
	ds_write_b128 v123, v[78:81] offset:192
	v_pk_fma_f32 v[90:91], v[90:91], v[76:77], v[236:237] op_sel_hi:[1,0,0]
	v_pk_fma_f32 v[92:93], v[92:93], v[76:77], v[236:237] op_sel_hi:[1,0,0]
	ds_write_b128 v123, v[86:89] offset:256
	v_pk_fma_f32 v[148:149], v[148:149], v[76:77], v[236:237] op_sel_hi:[1,0,0]
	v_pk_fma_f32 v[150:151], v[150:151], v[76:77], v[236:237] op_sel_hi:[1,0,0]
	ds_write_b128 v123, v[90:93] offset:320
	v_pk_fma_f32 v[82:83], v[82:83], v[76:77], v[236:237] op_sel_hi:[1,0,0]
	v_pk_fma_f32 v[84:85], v[84:85], v[76:77], v[236:237] op_sel_hi:[1,0,0]
	ds_write_b128 v123, v[148:151] offset:384
	ds_write_b128 v123, v[82:85] offset:448
	ds_read_b128 v[62:65], v121
	ds_read_b128 v[66:69], v121 offset:1088
	ds_read_b128 v[70:73], v121 offset:2176
	ds_read_b128 v[74:77], v121 offset:3264
	ds_read_b128 v[78:81], v121 offset:4352
	ds_read_b128 v[82:85], v121 offset:5440
	ds_read_b128 v[86:89], v121 offset:6528
	ds_read_b128 v[90:93], v121 offset:7616
	v_add_u32_e32 v136, 0xffffe400, v118
	s_waitcnt vmcnt(15) lgkmcnt(7)
	v_pk_fma_f32 v[64:65], v[56:57], v[64:65], v[60:61]
	v_pk_fma_f32 v[62:63], v[54:55], v[62:63], v[58:59]
	buffer_store_dwordx4 v[62:65], v136, s[4:7], 0 offen sc0 nt sc1
	v_cmp_lt_i32_e32 vcc, s8, v0
	s_or_b64 s[0:1], vcc, s[0:1]
	s_waitcnt lgkmcnt(6)
	v_pk_fma_f32 v[64:65], v[56:57], v[68:69], v[60:61]
	v_pk_fma_f32 v[62:63], v[54:55], v[66:67], v[58:59]
	v_add_u32_e32 v66, 0xffffe800, v118
	buffer_store_dwordx4 v[62:65], v66, s[4:7], 0 offen sc0 nt sc1
	v_add_u32_e32 v66, 0xffffec00, v118
	s_waitcnt lgkmcnt(5)
	v_pk_fma_f32 v[64:65], v[56:57], v[72:73], v[60:61]
	v_pk_fma_f32 v[62:63], v[54:55], v[70:71], v[58:59]
	buffer_store_dwordx4 v[62:65], v66, s[4:7], 0 offen sc0 nt sc1
	v_add_u32_e32 v66, 0xfffff000, v118
	s_waitcnt lgkmcnt(4)
	v_pk_fma_f32 v[64:65], v[56:57], v[76:77], v[60:61]
	v_pk_fma_f32 v[62:63], v[54:55], v[74:75], v[58:59]
	buffer_store_dwordx4 v[62:65], v66, s[4:7], 0 offen sc0 nt sc1
	v_add_u32_e32 v66, 0xfffff400, v118
	s_waitcnt lgkmcnt(3)
	v_pk_fma_f32 v[64:65], v[56:57], v[80:81], v[60:61]
	v_pk_fma_f32 v[62:63], v[54:55], v[78:79], v[58:59]
	buffer_store_dwordx4 v[62:65], v66, s[4:7], 0 offen sc0 nt sc1
	v_add_u32_e32 v66, 0xfffff800, v118
	s_waitcnt lgkmcnt(2)
	v_pk_fma_f32 v[64:65], v[56:57], v[84:85], v[60:61]
	v_pk_fma_f32 v[62:63], v[54:55], v[82:83], v[58:59]
	buffer_store_dwordx4 v[62:65], v66, s[4:7], 0 offen sc0 nt sc1
	v_add_u32_e32 v66, 0xfffffc00, v118
	s_waitcnt lgkmcnt(1)
	v_pk_fma_f32 v[64:65], v[56:57], v[88:89], v[60:61]
	v_pk_fma_f32 v[62:63], v[54:55], v[86:87], v[58:59]
	buffer_store_dwordx4 v[62:65], v66, s[4:7], 0 offen sc0 nt sc1
	s_waitcnt lgkmcnt(0)
	s_nop 0
	v_pk_fma_f32 v[64:65], v[56:57], v[92:93], v[60:61]
	v_pk_fma_f32 v[62:63], v[54:55], v[90:91], v[58:59]
	buffer_store_dwordx4 v[62:65], v118, s[4:7], 0 offen sc0 nt sc1
	v_add_u32_e32 v118, 0x1000000, v118
	s_nop 0
	v_mov_b32_e32 v62, v0
	s_waitcnt vmcnt(21)
	v_mov_b32_e32 v64, v135
	s_andn2_b64 exec, exec, s[0:1]
	s_cbranch_execnz .LBB1_6

	.amdhsa_kernel _Z9edge_mainPKfS0_PKiS2_PKcPcS0_S0_Pf
		.amdhsa_group_segment_fixed_size 156160
		.amdhsa_private_segment_fixed_size 0
		.amdhsa_kernarg_size 72
		.amdhsa_user_sgpr_count 2
		.amdhsa_user_sgpr_dispatch_ptr 0
		.amdhsa_user_sgpr_queue_ptr 0
		.amdhsa_user_sgpr_kernarg_segment_ptr 1
		.amdhsa_user_sgpr_dispatch_id 0
		.amdhsa_user_sgpr_kernarg_preload_length 0
		.amdhsa_user_sgpr_kernarg_preload_offset 0
		.amdhsa_user_sgpr_private_segment_size 0
		.amdhsa_uses_dynamic_stack 0
		.amdhsa_enable_private_segment 0
		.amdhsa_system_sgpr_workgroup_id_x 1
		.amdhsa_system_sgpr_workgroup_id_y 0
		.amdhsa_system_sgpr_workgroup_id_z 0
		.amdhsa_system_sgpr_workgroup_info 0
		.amdhsa_system_vgpr_workitem_id 0
		.amdhsa_next_free_vgpr 240
		.amdhsa_next_free_sgpr 96
		.amdhsa_accum_offset 240
		.amdhsa_reserve_vcc 1
		.amdhsa_float_round_mode_32 0
		.amdhsa_float_round_mode_16_64 0
		.amdhsa_float_denorm_mode_32 3
		.amdhsa_float_denorm_mode_16_64 3
		.amdhsa_dx10_clamp 1
		.amdhsa_ieee_mode 1
		.amdhsa_fp16_overflow 0
		.amdhsa_tg_split 0
		.amdhsa_exception_fp_ieee_invalid_op 0
		.amdhsa_exception_fp_denorm_src 0
		.amdhsa_exception_fp_ieee_div_zero 0
		.amdhsa_exception_fp_ieee_overflow 0
		.amdhsa_exception_fp_ieee_underflow 0
		.amdhsa_exception_fp_ieee_inexact 0
		.amdhsa_exception_int_div_zero 0
	.end_amdhsa_kernel

amdhsa.kernels:
  - .agpr_count:     0
    .args:
      - .actual_access:  read_only
        .address_space:  global
        .offset:         0
        .size:           8
        .value_kind:     global_buffer
      - .actual_access:  read_only
        .address_space:  global
        .offset:         8
        .size:           8
        .value_kind:     global_buffer
      - .actual_access:  read_only
        .address_space:  global
        .offset:         16
        .size:           8
        .value_kind:     global_buffer
      - .actual_access:  read_only
        .address_space:  global
        .offset:         24
        .size:           8
        .value_kind:     global_buffer
      - .actual_access:  read_only
        .address_space:  global
        .offset:         32
        .size:           8
        .value_kind:     global_buffer
      - .actual_access:  write_only
        .address_space:  global
        .offset:         40
        .size:           8
        .value_kind:     global_buffer
    .group_segment_fixed_size: 157696
    .kernarg_segment_align: 8
    .kernarg_segment_size: 48
    .language:       OpenCL C
    .language_version:
      - 2
      - 0
    .max_flat_workgroup_size: 512
    .name:           _Z4prepPKfS0_S0_S0_S0_Pc
    .private_segment_fixed_size: 0
    .sgpr_count:     36
    .sgpr_spill_count: 0
    .symbol:         _Z4prepPKfS0_S0_S0_S0_Pc.kd
    .uniform_work_group_size: 1
    .uses_dynamic_stack: false
    .vgpr_count:     256
    .vgpr_spill_count: 0
    .wavefront_size: 64
  - .agpr_count:     0
    .args:
      - .actual_access:  read_only
        .address_space:  global
        .offset:         0
        .size:           8
        .value_kind:     global_buffer
      - .actual_access:  read_only
        .address_space:  global
        .offset:         8
        .size:           8
        .value_kind:     global_buffer
      - .actual_access:  read_only
        .address_space:  global
        .offset:         16
        .size:           8
        .value_kind:     global_buffer
      - .actual_access:  read_only
        .address_space:  global
        .offset:         24
        .size:           8
        .value_kind:     global_buffer
      - .actual_access:  read_only
        .address_space:  global
        .offset:         32
        .size:           8
        .value_kind:     global_buffer
      - .actual_access:  write_only
        .address_space:  global
        .offset:         40
        .size:           8
        .value_kind:     global_buffer
      - .actual_access:  read_only
        .address_space:  global
        .offset:         48
        .size:           8
        .value_kind:     global_buffer
      - .actual_access:  read_only
        .address_space:  global
        .offset:         56
        .size:           8
        .value_kind:     global_buffer
      - .actual_access:  write_only
        .address_space:  global
        .offset:         64
        .size:           8
        .value_kind:     global_buffer
    .group_segment_fixed_size: 156160
    .kernarg_segment_align: 8
    .kernarg_segment_size: 72
    .language:       OpenCL C
    .language_version:
      - 2
      - 0
    .max_flat_workgroup_size: 512
    .name:           _Z9edge_mainPKfS0_PKiS2_PKcPcS0_S0_Pf
    .private_segment_fixed_size: 0
    .sgpr_count:     22
    .sgpr_spill_count: 0
    .symbol:         _Z9edge_mainPKfS0_PKiS2_PKcPcS0_S0_Pf.kd
    .uniform_work_group_size: 1
    .uses_dynamic_stack: false
    .vgpr_count:     240
    .vgpr_spill_count: 0
    .wavefront_size: 64
